# attention phase (diff + swa work queues): static s_setprio 1 for waves 4-7
# baseline (speedup 1.0000x reference)
; __device__ __forceinline__ int lt_tid(int wv) { int ln; asm volatile("v_mbcnt_lo_u32_b32 %0, -1, 0\n\tv_mbcnt_hi_u32_b32 %0, -1, %0" : "=v"(ln)); return (wv << 6) | ln; }
; __device__ __forceinline__ unsigned char* lt_ptr(unsigned char* q) { unsigned long long a = (unsigned long long)q; asm volatile("" : "+s"(a)); return (unsigned char*)(GAS unsigned char*)a; }
; __device__ __forceinline__ void ph_rwkv_scan2(const Params& p, int l, LAS unsigned char* lds, int first_block, const int wvid) {
;     ...
;     const int tid = lt_tid(wvid), lane = tid & 63, wave = __builtin_amdgcn_readfirstlane(tid >> 6), l31 = lane & 31, hi = lane >> 5;
;     const int sw = (bid - first_block) * 4 + wave;
;     if (bid < first_block) return;
;     {
;         if (tid == 0) { unsigned* r2d = (unsigned*)(lt_ptr(p.ws) + WS_CTL) + CW_R2D + l * 64; unsigned sp = 0;
;             while (__hip_atomic_load(r2d, __ATOMIC_RELAXED, __HIP_MEMORY_SCOPE_AGENT) < gridDim.x) { __builtin_amdgcn_s_sleep(2); if (++sp > (1u << 24)) break; }
;             __builtin_amdgcn_fence(__ATOMIC_ACQUIRE, "agent"); asm volatile("s_waitcnt vmcnt(0)" ::: "memory"); }
;         __syncthreads();
;     }
;     if (wave >= 4) {
;         if ((int)gridDim.x * NWAVE == NB * 4 * 64 && wave < 6) r4_zero_state(p, l, lt_ptr(p.ws), ob, (bid - first_block) * 2 + (wave - 4), lane);
;         return; }
;     if (sw >= 64) return;
;     const int bh = sw >> 1, ib = sw & 1;
;     const bf16_t* PT = (const bf16_t*)(ob + RO_PT) + (size_t)bh * RCH * 4096; const bf16_t* QT = (const bf16_t*)(ob + RO_QT) + (size_t)bh * RCH * 4096;
;     u32x4* SH = (u32x4*)(ob + RO_SH) + (size_t)bh * RCH * 512;
;     bf16x8 Sp[4];
;     { unsigned z; asm volatile("v_mov_b32 %0, 0" : "=v"(z));
; #pragma unroll
;       for (int ks = 0; ks < 4; ++ks) { u32x4 zz; zz.x = z; zz.y = z; zz.z = z; zz.w = z; Sp[ks] = __builtin_bit_cast(bf16x8, zz); } }
;     bf16x8 Pf[2][4]; unsigned short Qi[2][16];
;     ...
;     R3_LOAD(0);
.LBB0_747:
	s_or_b64 exec, exec, s[0:1]
	s_cmp_lt_u32 s74, 0x100
	s_cbranch_scc1 .Lattn_prio_skip
	s_setprio 1
.Lattn_prio_skip:
	v_readlane_b32 s0, v254, 14
	s_ashr_i32 s8, s10, 6
	s_sub_i32 s9, s9, s0
	v_and_b32_e32 v106, 63, v104
	v_and_b32_e32 v105, 31, v104
	s_cmp_lt_i32 s8, 4
	s_mov_b64 s[0:1], -1
	s_barrier
	s_cbranch_scc0 .LBB0_756
	s_lshl_b32 s0, s9, 2
	s_add_i32 s0, s8, s0
	s_cmp_gt_i32 s0, 63
	s_cbranch_scc1 .LBB0_755
	s_waitcnt vmcnt(31)
	v_lshlrev_b32_e32 v2, 6, v105
	v_lshrrev_b32_e32 v0, 5, v106
	s_ashr_i32 s0, s0, 1
	s_bfe_u32 s10, s10, 0x10006
	v_and_b32_e32 v2, 0x400, v2
	s_mul_hi_i32 s1, s0, 0x82000
	s_mul_i32 s0, s0, 0x82000
	v_lshl_or_b32 v2, s10, 11, v2
	s_waitcnt vmcnt(30)
	v_lshlrev_b32_e32 v3, 6, v0
	s_waitcnt vmcnt(29)
	v_and_b32_e32 v4, 15, v104
	s_add_u32 s0, s2, s0
	v_or3_b32 v3, v2, v3, v4
	s_addc_u32 s1, s3, s1
	s_waitcnt vmcnt(27)
	v_lshlrev_b32_e32 v6, 1, v3
	s_waitcnt vmcnt(26)
	v_mov_b32_e32 v7, v1
	v_lshlrev_b32_e32 v2, 5, v105
	v_lshl_add_u64 v[92:93], s[0:1], 0, v[6:7]
	s_mov_b64 s[6:7], 0x6180000
	s_add_u32 s4, s0, 0x5140000
	v_lshl_or_b32 v0, v0, 4, v2
	v_lshl_add_u64 v[6:7], v[92:93], 0, s[6:7]
	s_mov_b32 s6, 0x6180000
	s_addc_u32 s5, s1, 0
	v_or_b32_e32 v2, 0x1000, v0
	s_waitcnt vmcnt(25)
	v_add_co_u32_e32 v8, vcc, s6, v92
	s_waitcnt vmcnt(23)
	v_or_b32_e32 v10, 0x1400, v0
	v_mov_b32 v34, 0
	v_or_b32_e32 v4, 0x1800, v0
	global_load_dwordx4 v[46:49], v2, s[4:5]
	global_load_dwordx4 v[42:45], v4, s[4:5]
	v_addc_co_u32_e32 v9, vcc, 0, v93, vcc
	global_load_ushort v107, v[6:7], off offset:32
	global_load_ushort v108, v[6:7], off offset:64
	global_load_ushort v109, v[6:7], off offset:96
	global_load_ushort v110, v[6:7], off offset:256
	global_load_ushort v111, v[6:7], off offset:288
	global_load_ushort v112, v[6:7], off offset:320
	global_load_ushort v113, v[6:7], off offset:352
	global_load_ushort v114, v[6:7], off offset:512
	global_load_dwordx4 v[78:81], v0, s[4:5]
	global_load_dwordx4 v[62:65], v0, s[4:5] offset:1024
	global_load_dwordx4 v[74:77], v0, s[4:5] offset:2048
	global_load_dwordx4 v[58:61], v0, s[4:5] offset:3072
	s_waitcnt vmcnt(35)
	v_or_b32_e32 v12, 0x1c00, v0
	global_load_dwordx4 v[50:53], v10, s[4:5]
	global_load_dwordx4 v[38:41], v12, s[4:5]
	global_load_ushort v122, v[6:7], off offset:544
	global_load_ushort v123, v[6:7], off offset:576
	global_load_ushort v124, v[6:7], off offset:608
	global_load_ushort v125, v[6:7], off offset:768
	global_load_ushort v126, v[6:7], off offset:800
	global_load_ushort v127, v[6:7], off offset:832
	global_load_ushort v128, v[6:7], off offset:864
	global_load_ushort v129, v[6:7], off offset:1024
	global_load_ushort v131, v[6:7], off offset:1056
	global_load_ushort v132, v[6:7], off offset:1088
	global_load_ushort v133, v[6:7], off offset:1120
	global_load_ushort v134, v[6:7], off offset:1280
	global_load_ushort v135, v[6:7], off offset:1312
	global_load_ushort v136, v[6:7], off offset:1344
	global_load_ushort v137, v[6:7], off offset:1376
	global_load_ushort v138, v[6:7], off offset:1536
	global_load_ushort v130, v[8:9], off
	global_load_ushort v115, v[6:7], off offset:1568
	global_load_ushort v116, v[6:7], off offset:1600
	global_load_ushort v117, v[6:7], off offset:1632
	global_load_ushort v118, v[6:7], off offset:1792
	global_load_ushort v119, v[6:7], off offset:1824
	global_load_ushort v120, v[6:7], off offset:1856
	global_load_ushort v121, v[6:7], off offset:1888
	v_lshlrev_b32_e32 v3, 4, v106
	s_add_u32 s4, s0, 0x5142000
	v_mov_b32_e32 v35, v34
	v_mov_b32_e32 v36, v34
	v_mov_b32_e32 v37, v34
	v_lshl_or_b32 v6, s10, 12, v3
	v_mov_b32_e32 v7, v1
	s_waitcnt vmcnt(60)
	v_mov_b32_e32 v13, v1
	s_addc_u32 s5, s1, 0
	v_mov_b32_e32 v11, v1
	v_mov_b32_e32 v5, v1
	v_mov_b32_e32 v3, v1
	s_waitcnt vmcnt(40)
	v_lshl_add_u64 v[90:91], s[0:1], 0, v[6:7]
	global_store_dwordx4 v6, v[34:37], s[0:1]
	global_store_dwordx4 v6, v[34:37], s[0:1] offset:1024
	global_store_dwordx4 v6, v[34:37], s[0:1] offset:2048
	global_store_dwordx4 v6, v[34:37], s[0:1] offset:3072
	v_lshl_add_u64 v[94:95], s[4:5], 0, v[12:13]
	v_lshl_add_u64 v[96:97], s[4:5], 0, v[10:11]
	v_lshl_add_u64 v[98:99], s[4:5], 0, v[4:5]
	v_lshl_add_u64 v[100:101], s[4:5], 0, v[2:3]
	v_lshl_add_u64 v[102:103], s[0:1], 0, v[0:1]
	s_mov_b64 s[0:1], 0
	v_mov_b32_e32 v54, v34
	v_mov_b32_e32 v55, v34
	v_mov_b32_e32 v56, v34
	v_mov_b32_e32 v57, v34
	v_mov_b32_e32 v66, v34
	v_mov_b32_e32 v67, v34
	v_mov_b32_e32 v68, v34
	v_mov_b32_e32 v69, v34
	v_mov_b32_e32 v70, v34
	v_mov_b32_e32 v71, v34
	v_mov_b32_e32 v72, v34
	v_mov_b32_e32 v73, v34
	s_movk_i32 s5, 0x2000

; #define LAS __attribute__((address_space(3)))
; __device__ __forceinline__ int lt_tid(int wv) { int ln; asm volatile("v_mbcnt_lo_u32_b32 %0, -1, 0\n\tv_mbcnt_hi_u32_b32 %0, -1, %0" : "=v"(ln)); return (wv << 6) | ln; }
; __device__ __forceinline__ int lt_bid() { int b = blockIdx.x; asm volatile("" : "+s"(b)); return b; }
; __device__ __forceinline__ unsigned char* lt_ptr(unsigned char* q) { unsigned long long a = (unsigned long long)q; asm volatile("" : "+s"(a)); return (unsigned char*)(GAS unsigned char*)a; }
; __device__ __forceinline__ void ph_rwkv_out(const Params& p, int l, LAS unsigned char* lds, const int wvid) {
;     const int bid = lt_bid(); unsigned char* const ws = lt_ptr(p.ws); unsigned char* const ob = lt_ptr((unsigned char*)p.out);
;     const int wave = __builtin_amdgcn_readfirstlane(lt_tid(wvid) >> 6);
;     bf16_t* MIX = (bf16_t*)(ws + WS_MIX);
;     const bf16_t* Gg = (const bf16_t*)(ws + WS_RWB + RW_G); const float* BCg = (const float*)(ws + WS_RWB + RW_BC);
;     {
;         if (lt_tid(wvid) == 0) { unsigned* scd = (unsigned*)(ws + WS_CTL) + CW_SCD + l * 64; unsigned sp = 0;
;             while (__hip_atomic_load(scd, __ATOMIC_RELAXED, __HIP_MEMORY_SCOPE_AGENT) < 64u) { __builtin_amdgcn_s_sleep(2); if (++sp > (1u << 24)) break; }
;             __builtin_amdgcn_fence(__ATOMIC_ACQUIRE, "agent"); asm volatile("s_waitcnt vmcnt(0)" ::: "memory"); }
;         __syncthreads();
;     }
.LBB0_835:
	s_setprio 0
	v_readlane_b32 s4, v253, 0
	v_readlane_b32 s6, v253, 2
	v_readlane_b32 s7, v253, 3
	s_mov_b32 s16, s65
	s_mov_b64 s[0:1], s[66:67]
	s_mov_b64 s[2:3], s[6:7]
	s_waitcnt lgkmcnt(0)
	s_barrier
	v_mbcnt_lo_u32_b32 v0, -1, 0
	v_mbcnt_hi_u32_b32 v0, -1, v0
	v_readlane_b32 s5, v253, 1
	v_or_b32_e32 v0, s75, v0
	s_nop 0
	v_readfirstlane_b32 s17, v0
	v_mbcnt_lo_u32_b32 v0, -1, 0
	v_mbcnt_hi_u32_b32 v0, -1, v0
	s_nop 0
	v_or_b32_e32 v0, s75, v0
	v_cmp_eq_u32_e32 vcc, 0, v0
	s_and_saveexec_b64 s[4:5], vcc
	s_cbranch_execz .LBB0_850
	s_add_u32 s6, s0, s10
	s_addc_u32 s7, s1, s11
	s_add_u32 s6, s6, 0x6400
	s_addc_u32 s7, s7, 0
	s_mov_b32 s10, 0x1000000
	s_branch .LBB0_839
